# grid barrier reads the workspace pointer from a VGPR lane cached at kernel start instead of a scalar kernarg load on the arrival path
# speedup vs baseline: 1.0032x; 1.0032x over previous
_Z7enc_fwd4Args:
	v_and_b32_e32 v1, 0x3ff, v0
	v_writelane_b32 v253, s2, 0
	s_load_dwordx2 s[2:3], s[0:1], 0xa0
	s_load_dword s76, s[0:1], 0xa8
	s_load_dwordx2 s[4:5], s[0:1], 0x98
	v_mbcnt_lo_u32_b32 v2, -1, 0
	v_mbcnt_hi_u32_b32 v2, -1, v2
	s_waitcnt lgkmcnt(0)
	v_writelane_b32 v255, s4, 62
	v_writelane_b32 v255, s5, 61
	v_writelane_b32 v253, s2, 1
	s_nop 1
	v_writelane_b32 v253, s3, 2
	v_readfirstlane_b32 s3, v1
	s_and_b32 s4, s3, 0xffffffc0
	v_writelane_b32 v253, s4, 3
	v_add_u32_e32 v2, s4, v2
	s_add_u32 s4, s0, 0xa8
	v_writelane_b32 v253, s0, 4
	s_addc_u32 s5, s1, 0
	s_mov_b32 s2, 0
	s_mov_b32 s100, 0
	v_writelane_b32 v253, s1, 5
	v_writelane_b32 v253, s4, 6
	v_cmp_gt_i32_e32 vcc, 2, v2
	s_nop 0
	v_writelane_b32 v253, s5, 7
	s_and_saveexec_b64 s[0:1], vcc
	v_lshl_add_u32 v3, v2, 2, 0
	v_add_u32_e32 v3, 0x20040, v3
	v_mov_b32_e32 v4, 0
	ds_write_b32 v3, v4
	s_or_b64 exec, exec, s[0:1]
	v_readlane_b32 s0, v253, 1
	v_readlane_b32 s1, v253, 2
	s_sub_i32 s0, s1, s0
	s_cmp_lt_i32 s0, 2
	s_waitcnt lgkmcnt(0)
	s_barrier
	s_cbranch_scc1 .LBB0_7
	s_getreg_b32 s0, hwreg(HW_REG_XCC_ID, 0, 4)
	s_and_b32 s2, s0, 15
	v_cmp_eq_u32_e32 vcc, 0, v2
	s_and_saveexec_b64 s[0:1], vcc
	s_cbranch_execz .LBB0_6
	s_mov_b64 s[4:5], exec
	v_mbcnt_lo_u32_b32 v2, s4, 0
	v_mbcnt_hi_u32_b32 v2, s5, v2
	v_cmp_eq_u32_e32 vcc, 0, v2
	s_and_b64 s[6:7], exec, vcc
	s_mov_b64 exec, s[6:7]
	s_cbranch_execz .LBB0_6
	v_readlane_b32 s6, v253, 4
	v_readlane_b32 s7, v253, 5
	s_load_dwordx2 s[6:7], s[6:7], 0x98
	s_lshl_b32 s8, s2, 8
	v_mov_b32_e32 v2, 0x4000
	s_waitcnt lgkmcnt(0)
	s_add_u32 s6, s6, s8
	s_addc_u32 s7, s7, 0
	s_bcnt1_i32_b64 s4, s[4:5]
	v_mov_b32_e32 v3, s4
	global_atomic_add v2, v3, s[6:7] offset:1024

.LBB0_1064:
	v_readlane_b32 s6, v253, 30
	v_readlane_b32 s7, v253, 31
	s_and_b64 vcc, exec, s[6:7]
	s_cbranch_vccz .LBB0_1114
	s_waitcnt vmcnt(0)
	v_cmp_eq_u32_e32 vcc, 0, v192
	s_waitcnt vmcnt(0) lgkmcnt(0)
	s_barrier
	s_and_saveexec_b64 s[4:5], vcc
	s_cbranch_execz .LBB0_1113
	v_readlane_b32 s6, v254, 59
	v_readlane_b32 s0, v255, 62
	v_readlane_b32 s1, v255, 61
	s_waitcnt vmcnt(0) expcnt(0) lgkmcnt(0)
	v_mov_b32_e32 v0, s6
	ds_read_b32 v3, v0
	v_readlane_b32 s6, v254, 60
	s_waitcnt lgkmcnt(0)
	v_cmp_ne_u32_e32 vcc, 0, v3
	v_mov_b32_e32 v0, s6
	ds_read_b32 v0, v0
	s_cbranch_vccnz .LBB0_1081
	s_add_u32 s26, s0, 0x4200
	s_addc_u32 s27, s1, 0
	s_add_u32 s30, s0, 0x4400
	s_addc_u32 s31, s1, 0
	s_add_u32 s36, s0, 0x4500
	s_addc_u32 s37, s1, 0
	s_add_u32 s38, s0, 0x4600
	s_addc_u32 s39, s1, 0
	s_add_u32 s40, s0, 0x4700
	s_addc_u32 s41, s1, 0
	s_add_u32 s42, s0, 0x4800
	s_addc_u32 s43, s1, 0
	s_add_u32 s44, s0, 0x4900
	s_addc_u32 s45, s1, 0
	s_add_u32 s46, s0, 0x4a00
	s_addc_u32 s47, s1, 0
	s_add_u32 s50, s0, 0x4b00
	s_addc_u32 s51, s1, 0
	s_add_u32 s52, s0, 0x4c00
	s_addc_u32 s53, s1, 0
	s_add_u32 s54, s0, 0x4d00
	s_addc_u32 s55, s1, 0
	s_add_u32 s56, s0, 0x4e00
	s_addc_u32 s57, s1, 0
	s_add_u32 s58, s0, 0x4f00
	v_readlane_b32 s14, v253, 6
	s_addc_u32 s59, s1, 0
	v_readlane_b32 s15, v253, 7
	s_add_u32 s60, s0, 0x5000
	s_load_dwordx2 s[6:7], s[14:15], 0x4
	s_addc_u32 s61, s1, 0
	s_add_u32 s62, s0, 0x5100
	s_addc_u32 s63, s1, 0
	s_add_u32 s64, s0, 0x5200
	s_addc_u32 s65, s1, 0
	s_waitcnt lgkmcnt(0)
	s_mul_i32 s6, s6, s76
	s_add_u32 s66, s0, 0x5300
	s_mul_i32 s6, s6, s7
	s_addc_u32 s67, s1, 0
	s_mov_b32 s14, 1
	s_branch .LBB0_1069
